# P1 epilogue stores without the nt cache hint (write-back in L2 instead of streaming)
# baseline (speedup 1.0000x reference)
.LBB0_204:
	v_lshl_add_u64 v[178:179], v[162:163], 1, v[166:167]
	v_cvt_pk_bf16_f32 v144, v160, v181
	v_cvt_pk_bf16_f32 v145, v182, v184
	v_cvt_pk_bf16_f32 v146, v165, v187
	v_cvt_pk_bf16_f32 v147, v188, v190
	s_and_b64 vcc, exec, s[6:7]
	s_mov_b64 s[6:7], -1
	global_store_dwordx4 v[178:179], v[144:147], off
	s_cbranch_vccnz .LBB0_206
	s_nop 0
	v_mov_b64_e32 v[146:147], v[114:115]
	v_mov_b64_e32 v[150:151], v[118:119]
	s_mov_b64 s[6:7], 0
	v_mov_b64_e32 v[144:145], v[112:113]
	v_mov_b64_e32 v[148:149], v[116:117]

.LBB0_213:
	v_or_b32_e32 v114, 16, v176
	v_mov_b64_e32 v[112:113], s[10:11]
	s_waitcnt vmcnt(0)
	v_mad_i64_i32 v[136:137], s[6:7], v114, s84, v[112:113]
	v_cndmask_b32_e64 v112, 0, 1, s[8:9]
	v_cmp_ne_u32_e64 s[6:7], 1, v112
	s_andn2_b64 vcc, exec, s[8:9]
	s_mov_b64 s[8:9], -1
	global_store_dwordx4 v[148:149], v[144:147], off
	s_cbranch_vccnz .LBB0_229
	v_mov_b64_e32 v[116:117], v[132:133]
	v_mov_b64_e32 v[112:113], v[128:129]
	s_and_b64 vcc, exec, s[4:5]
	v_mov_b64_e32 v[118:119], v[134:135]
	v_mov_b64_e32 v[114:115], v[130:131]
	s_cbranch_vccnz .LBB0_216
	v_or_b32_e32 v112, 32, v176
	v_ashrrev_i32_e32 v113, 31, v112
	v_lshlrev_b64 v[112:113], 7, v[112:113]
	v_lshl_add_u64 v[116:117], v[170:171], 0, v[112:113]
	global_load_dwordx4 v[112:115], v[116:117], off
	s_nop 0
	global_load_dwordx4 v[116:119], v[116:117], off offset:64

.LBB0_222:
	v_lshl_add_u64 v[138:139], v[162:163], 1, v[136:137]
	v_cvt_pk_bf16_f32 v120, v140, v141
	v_cvt_pk_bf16_f32 v121, v142, v144
	v_cvt_pk_bf16_f32 v122, v143, v147
	v_cvt_pk_bf16_f32 v123, v148, v150
	s_and_b64 vcc, exec, s[8:9]
	s_mov_b64 s[8:9], -1
	global_store_dwordx4 v[138:139], v[120:123], off
	s_cbranch_vccnz .LBB0_224
	s_nop 0
	v_mov_b64_e32 v[122:123], v[98:99]
	v_mov_b64_e32 v[126:127], v[102:103]
	s_mov_b64 s[8:9], 0
	v_mov_b64_e32 v[120:121], v[96:97]
	v_mov_b64_e32 v[124:125], v[100:101]

.LBB0_231:
	v_or_b32_e32 v98, 32, v176
	v_mov_b64_e32 v[96:97], s[10:11]
	global_store_dwordx4 v[124:125], v[120:123], off
	s_and_b64 vcc, exec, s[6:7]
	s_nop 0
	v_mad_i64_i32 v[120:121], s[8:9], v98, s84, v[96:97]
	s_mov_b64 s[8:9], -1
	s_cbranch_vccnz .LBB0_247
	s_waitcnt vmcnt(2)
	v_mov_b64_e32 v[100:101], v[116:117]
	v_mov_b64_e32 v[96:97], v[112:113]
	s_and_b64 vcc, exec, s[4:5]
	v_mov_b64_e32 v[102:103], v[118:119]
	v_mov_b64_e32 v[98:99], v[114:115]
	s_cbranch_vccnz .LBB0_234
	v_or_b32_e32 v96, 48, v176
	v_ashrrev_i32_e32 v97, 31, v96
	v_lshlrev_b64 v[96:97], 7, v[96:97]
	v_lshl_add_u64 v[100:101], v[170:171], 0, v[96:97]
	global_load_dwordx4 v[96:99], v[100:101], off
	s_nop 0
	global_load_dwordx4 v[100:103], v[100:101], off offset:64

.LBB0_240:
	v_lshl_add_u64 v[122:123], v[162:163], 1, v[120:121]
	v_cvt_pk_bf16_f32 v104, v124, v125
	v_cvt_pk_bf16_f32 v105, v126, v128
	v_cvt_pk_bf16_f32 v106, v127, v131
	v_cvt_pk_bf16_f32 v107, v132, v134
	s_and_b64 vcc, exec, s[8:9]
	s_mov_b64 s[8:9], -1
	global_store_dwordx4 v[122:123], v[104:107], off
	s_cbranch_vccnz .LBB0_242
	s_nop 0
	v_mov_b64_e32 v[106:107], v[82:83]
	v_mov_b64_e32 v[110:111], v[86:87]
	s_mov_b64 s[8:9], 0
	v_mov_b64_e32 v[104:105], v[80:81]
	v_mov_b64_e32 v[108:109], v[84:85]

.LBB0_249:
	v_or_b32_e32 v82, 48, v176
	v_mov_b64_e32 v[80:81], s[10:11]
	global_store_dwordx4 v[108:109], v[104:107], off
	s_and_b64 vcc, exec, s[6:7]
	s_nop 0
	v_mad_i64_i32 v[104:105], s[8:9], v82, s84, v[80:81]
	s_mov_b64 s[8:9], -1
	s_cbranch_vccnz .LBB0_265
	s_waitcnt vmcnt(2)
	v_mov_b64_e32 v[84:85], v[100:101]
	v_mov_b64_e32 v[80:81], v[96:97]
	s_and_b64 vcc, exec, s[4:5]
	v_mov_b64_e32 v[86:87], v[102:103]
	v_mov_b64_e32 v[82:83], v[98:99]
	s_cbranch_vccnz .LBB0_252
	v_lshlrev_b64 v[80:81], 7, v[176:177]
	v_lshl_add_u64 v[80:81], v[170:171], 0, v[80:81]
	s_mov_b64 s[8:9], 0x4000
	v_lshl_add_u64 v[84:85], v[80:81], 0, s[8:9]
	v_add_co_u32_e32 v80, vcc, 0x4000, v80
	s_nop 1
	v_addc_co_u32_e32 v81, vcc, 0, v81, vcc
	global_load_dwordx4 v[80:83], v[80:81], off
	s_nop 0
	global_load_dwordx4 v[84:87], v[84:85], off offset:64

.LBB0_258:
	v_lshl_add_u64 v[106:107], v[162:163], 1, v[104:105]
	v_cvt_pk_bf16_f32 v88, v108, v109
	v_cvt_pk_bf16_f32 v89, v110, v112
	v_cvt_pk_bf16_f32 v90, v111, v115
	v_cvt_pk_bf16_f32 v91, v116, v118
	s_and_b64 vcc, exec, s[8:9]
	s_mov_b64 s[8:9], -1
	global_store_dwordx4 v[106:107], v[88:91], off
	s_cbranch_vccnz .LBB0_260
	s_nop 0
	v_mov_b64_e32 v[90:91], v[66:67]
	v_mov_b64_e32 v[94:95], v[70:71]
	s_mov_b64 s[8:9], 0
	v_mov_b64_e32 v[88:89], v[64:65]
	v_mov_b64_e32 v[92:93], v[68:69]

.LBB0_267:
	v_add_u32_e32 v104, 0x80, v176
	v_mov_b64_e32 v[64:65], s[10:11]
	global_store_dwordx4 v[92:93], v[88:91], off
	s_and_b64 vcc, exec, s[6:7]
	s_nop 0
	v_mad_i64_i32 v[88:89], s[8:9], v104, s84, v[64:65]
	s_mov_b64 s[8:9], -1
	s_cbranch_vccnz .LBB0_283
	s_waitcnt vmcnt(2)
	v_mov_b64_e32 v[68:69], v[84:85]
	v_mov_b64_e32 v[64:65], v[80:81]
	s_and_b64 vcc, exec, s[4:5]
	v_mov_b64_e32 v[70:71], v[86:87]
	v_mov_b64_e32 v[66:67], v[82:83]
	s_cbranch_vccnz .LBB0_270
	v_or_b32_e32 v64, 16, v104
	v_ashrrev_i32_e32 v65, 31, v64
	v_lshlrev_b64 v[64:65], 7, v[64:65]
	v_lshl_add_u64 v[68:69], v[170:171], 0, v[64:65]
	global_load_dwordx4 v[64:67], v[68:69], off
	s_nop 0
	global_load_dwordx4 v[68:71], v[68:69], off offset:64

.LBB0_276:
	v_lshl_add_u64 v[90:91], v[162:163], 1, v[88:89]
	v_cvt_pk_bf16_f32 v72, v92, v93
	v_cvt_pk_bf16_f32 v73, v94, v96
	v_cvt_pk_bf16_f32 v74, v95, v99
	v_cvt_pk_bf16_f32 v75, v100, v102
	s_and_b64 vcc, exec, s[8:9]
	s_mov_b64 s[8:9], -1
	global_store_dwordx4 v[90:91], v[72:75], off
	s_cbranch_vccnz .LBB0_278
	s_nop 0
	v_mov_b64_e32 v[74:75], v[50:51]
	v_mov_b64_e32 v[78:79], v[54:55]
	s_mov_b64 s[8:9], 0
	v_mov_b64_e32 v[72:73], v[48:49]
	v_mov_b64_e32 v[76:77], v[52:53]

.LBB0_285:
	v_add_u32_e32 v50, 0x90, v176
	v_mov_b64_e32 v[48:49], s[10:11]
	global_store_dwordx4 v[76:77], v[72:75], off
	s_and_b64 vcc, exec, s[6:7]
	s_nop 0
	v_mad_i64_i32 v[72:73], s[8:9], v50, s84, v[48:49]
	s_mov_b64 s[8:9], -1
	s_cbranch_vccnz .LBB0_301
	s_waitcnt vmcnt(2)
	v_mov_b64_e32 v[52:53], v[68:69]
	v_mov_b64_e32 v[48:49], v[64:65]
	s_and_b64 vcc, exec, s[4:5]
	v_mov_b64_e32 v[54:55], v[70:71]
	v_mov_b64_e32 v[50:51], v[66:67]
	s_cbranch_vccnz .LBB0_288
	v_or_b32_e32 v48, 32, v104
	v_ashrrev_i32_e32 v49, 31, v48
	v_lshlrev_b64 v[48:49], 7, v[48:49]
	v_lshl_add_u64 v[52:53], v[170:171], 0, v[48:49]
	global_load_dwordx4 v[48:51], v[52:53], off
	s_nop 0
	global_load_dwordx4 v[52:55], v[52:53], off offset:64

.LBB0_294:
	v_lshl_add_u64 v[74:75], v[162:163], 1, v[72:73]
	v_cvt_pk_bf16_f32 v56, v76, v77
	v_cvt_pk_bf16_f32 v57, v78, v80
	v_cvt_pk_bf16_f32 v58, v79, v83
	v_cvt_pk_bf16_f32 v59, v84, v86
	s_and_b64 vcc, exec, s[8:9]
	s_mov_b64 s[8:9], -1
	global_store_dwordx4 v[74:75], v[56:59], off
	s_cbranch_vccnz .LBB0_296
	s_nop 0
	v_mov_b64_e32 v[58:59], v[34:35]
	v_mov_b64_e32 v[62:63], v[38:39]
	s_mov_b64 s[8:9], 0
	v_mov_b64_e32 v[56:57], v[32:33]
	v_mov_b64_e32 v[60:61], v[36:37]

.LBB0_303:
	v_add_u32_e32 v34, 0xa0, v176
	v_mov_b64_e32 v[32:33], s[10:11]
	global_store_dwordx4 v[60:61], v[56:59], off
	s_and_b64 vcc, exec, s[6:7]
	s_nop 0
	v_mad_i64_i32 v[56:57], s[8:9], v34, s84, v[32:33]
	s_mov_b64 s[8:9], -1
	s_cbranch_vccnz .LBB0_319
	s_waitcnt vmcnt(2)
	v_mov_b64_e32 v[36:37], v[52:53]
	v_mov_b64_e32 v[32:33], v[48:49]
	s_and_b64 vcc, exec, s[4:5]
	v_mov_b64_e32 v[38:39], v[54:55]
	v_mov_b64_e32 v[34:35], v[50:51]
	s_cbranch_vccnz .LBB0_306
	v_or_b32_e32 v32, 48, v104
	v_ashrrev_i32_e32 v33, 31, v32
	v_lshlrev_b64 v[32:33], 7, v[32:33]
	v_lshl_add_u64 v[36:37], v[170:171], 0, v[32:33]
	global_load_dwordx4 v[32:35], v[36:37], off
	s_nop 0
	global_load_dwordx4 v[36:39], v[36:37], off offset:64

.LBB0_312:
	v_lshl_add_u64 v[58:59], v[162:163], 1, v[56:57]
	v_cvt_pk_bf16_f32 v40, v60, v61
	v_cvt_pk_bf16_f32 v41, v62, v64
	v_cvt_pk_bf16_f32 v42, v63, v67
	v_cvt_pk_bf16_f32 v43, v68, v70
	s_and_b64 vcc, exec, s[8:9]
	s_mov_b64 s[8:9], -1
	global_store_dwordx4 v[58:59], v[40:43], off
	s_cbranch_vccnz .LBB0_314
	s_nop 0
	v_mov_b64_e32 v[42:43], v[18:19]
	v_mov_b64_e32 v[46:47], v[22:23]
	s_mov_b64 s[8:9], 0
	v_mov_b64_e32 v[40:41], v[16:17]
	v_mov_b64_e32 v[44:45], v[20:21]

.LBB0_321:
	v_add_u32_e32 v18, 0xb0, v176
	v_mov_b64_e32 v[16:17], s[10:11]
	v_mad_i64_i32 v[24:25], s[8:9], v18, s84, v[16:17]
	s_and_b64 vcc, exec, s[6:7]
	s_mov_b64 s[6:7], -1
	global_store_dwordx4 v[44:45], v[40:43], off
	s_cbranch_vccz .LBB0_324
	s_and_b64 vcc, exec, s[6:7]
	s_cbranch_vccnz .LBB0_337
.LBB0_323:
	s_andn2_b64 vcc, exec, s[2:3]
	s_mov_b64 s[2:3], -1
	global_store_dwordx4 v[20:21], v[16:19], off
	s_cbranch_vccnz .LBB0_185
	s_branch .LBB0_338

.LBB0_330:
	v_lshl_add_u64 v[26:27], v[162:163], 1, v[24:25]
	v_cvt_pk_bf16_f32 v16, v28, v29
	v_cvt_pk_bf16_f32 v17, v30, v40
	v_cvt_pk_bf16_f32 v18, v31, v43
	v_cvt_pk_bf16_f32 v19, v44, v46
	s_and_b64 vcc, exec, s[6:7]
	s_mov_b64 s[6:7], -1
	global_store_dwordx4 v[26:27], v[16:19], off
	s_cbranch_vccnz .LBB0_332
	s_nop 0
	v_mov_b64_e32 v[18:19], v[2:3]
	v_mov_b64_e32 v[22:23], v[6:7]
	s_mov_b64 s[6:7], 0
	v_mov_b64_e32 v[16:17], v[0:1]
	v_mov_b64_e32 v[20:21], v[4:5]

.LBB0_337:
	v_mul_f32_e32 v4, 0xbfb8aa3b, v4
	v_exp_f32_e32 v4, v4
	v_mul_f32_e32 v5, 0xbfb8aa3b, v5
	v_exp_f32_e32 v5, v5
	v_mul_f32_e32 v12, 0xbfb8aa3b, v12
	v_mul_f32_e32 v8, 0xbfb8aa3b, v8
	v_exp_f32_e32 v12, v12
	v_mul_f32_e32 v13, 0xbfb8aa3b, v13
	v_exp_f32_e32 v8, v8
	v_mul_f32_e32 v9, 0xbfb8aa3b, v9
	v_exp_f32_e32 v13, v13
	v_exp_f32_e32 v9, v9
	v_add_f32_e32 v4, 1.0, v4
	v_rcp_f32_e32 v4, v4
	v_add_f32_e32 v5, 1.0, v5
	v_mul_f32_e32 v0, 0xbfb8aa3b, v0
	v_rcp_f32_e32 v5, v5
	v_add_f32_e32 v12, 1.0, v12
	v_add_f32_e32 v8, 1.0, v8
	v_exp_f32_e32 v0, v0
	v_mul_f32_e32 v1, 0xbfb8aa3b, v1
	v_rcp_f32_e32 v12, v12
	v_rcp_f32_e32 v8, v8
	v_add_f32_e32 v13, 1.0, v13
	v_add_f32_e32 v9, 1.0, v9
	v_exp_f32_e32 v1, v1
	v_rcp_f32_e32 v13, v13
	v_rcp_f32_e32 v9, v9
	v_mul_f32_e32 v4, 0x437f0000, v4
	v_rndne_f32_e32 v4, v4
	v_mul_f32_e32 v5, 0x437f0000, v5
	v_max_f32_e32 v4, 1.0, v4
	v_add_f32_e32 v0, 1.0, v0
	v_rndne_f32_e32 v5, v5
	v_mul_f32_e32 v12, 0x437f0000, v12
	v_mul_f32_e32 v8, 0x437f0000, v8
	v_rcp_f32_e32 v0, v0
	v_cvt_pk_u8_f32 v4, v4, 0, 0
	v_max_f32_e32 v5, 1.0, v5
	v_add_f32_e32 v1, 1.0, v1
	v_rndne_f32_e32 v12, v12
	v_rndne_f32_e32 v8, v8
	v_mul_f32_e32 v13, 0x437f0000, v13
	v_mul_f32_e32 v9, 0x437f0000, v9
	v_rcp_f32_e32 v1, v1
	v_cvt_pk_u8_f32 v4, v5, 1, v4
	v_mul_f32_e32 v5, 0xbfb8aa3b, v6
	v_max_f32_e32 v12, 1.0, v12
	v_max_f32_e32 v8, 1.0, v8
	v_rndne_f32_e32 v13, v13
	v_rndne_f32_e32 v9, v9
	v_exp_f32_e32 v5, v5
	v_cvt_pk_u8_f32 v12, v12, 0, 0
	v_cvt_pk_u8_f32 v8, v8, 0, 0
	v_max_f32_e32 v13, 1.0, v13
	v_max_f32_e32 v9, 1.0, v9
	v_cvt_pk_u8_f32 v12, v13, 1, v12
	v_mul_f32_e32 v13, 0xbfb8aa3b, v14
	v_cvt_pk_u8_f32 v8, v9, 1, v8
	v_mul_f32_e32 v9, 0xbfb8aa3b, v10
	v_mul_f32_e32 v0, 0x437f0000, v0
	v_exp_f32_e32 v13, v13
	v_exp_f32_e32 v9, v9
	v_rndne_f32_e32 v0, v0
	v_mul_f32_e32 v1, 0x437f0000, v1
	v_max_f32_e32 v0, 1.0, v0
	v_rndne_f32_e32 v1, v1
	v_add_f32_e32 v5, 1.0, v5
	v_cvt_pk_u8_f32 v0, v0, 0, 0
	v_max_f32_e32 v1, 1.0, v1
	v_rcp_f32_e32 v5, v5
	v_cvt_pk_u8_f32 v0, v1, 1, v0
	v_mul_f32_e32 v1, 0xbfb8aa3b, v2
	v_add_f32_e32 v13, 1.0, v13
	v_add_f32_e32 v9, 1.0, v9
	v_exp_f32_e32 v1, v1
	v_rcp_f32_e32 v13, v13
	v_rcp_f32_e32 v9, v9
	v_mul_f32_e32 v2, 0x437f0000, v5
	v_mul_f32_e32 v5, 0xbfb8aa3b, v7
	v_exp_f32_e32 v5, v5
	v_add_f32_e32 v1, 1.0, v1
	v_mul_f32_e32 v10, 0x437f0000, v13
	v_mul_f32_e32 v9, 0x437f0000, v9
	v_rndne_f32_e32 v2, v2
	v_rcp_f32_e32 v1, v1
	v_mul_f32_e32 v3, 0xbfb8aa3b, v3
	v_rndne_f32_e32 v10, v10
	v_rndne_f32_e32 v9, v9
	v_max_f32_e32 v2, 1.0, v2
	v_exp_f32_e32 v3, v3
	v_max_f32_e32 v10, 1.0, v10
	v_max_f32_e32 v9, 1.0, v9
	v_cvt_pk_u8_f32 v2, v2, 2, v4
	v_add_f32_e32 v4, 1.0, v5
	v_cvt_pk_u8_f32 v10, v10, 2, v12
	v_mul_f32_e32 v12, 0xbfb8aa3b, v15
	v_cvt_pk_u8_f32 v8, v9, 2, v8
	v_mul_f32_e32 v9, 0xbfb8aa3b, v11
	v_rcp_f32_e32 v4, v4
	v_exp_f32_e32 v12, v12
	v_exp_f32_e32 v9, v9
	v_mul_f32_e32 v1, 0x437f0000, v1
	v_rndne_f32_e32 v1, v1
	v_add_f32_e32 v3, 1.0, v3
	v_max_f32_e32 v1, 1.0, v1
	v_rcp_f32_e32 v3, v3
	v_cvt_pk_u8_f32 v0, v1, 2, v0
	v_mul_f32_e32 v1, 0x437f0000, v4
	v_add_f32_e32 v12, 1.0, v12
	v_add_f32_e32 v9, 1.0, v9
	v_rndne_f32_e32 v1, v1
	v_rcp_f32_e32 v12, v12
	v_rcp_f32_e32 v9, v9
	v_max_f32_e32 v1, 1.0, v1
	v_cvt_pk_u8_f32 v18, v1, 3, v2
	v_mul_f32_e32 v1, 0x437f0000, v3
	v_rndne_f32_e32 v1, v1
	v_max_f32_e32 v1, 1.0, v1
	v_mul_f32_e32 v11, 0x437f0000, v12
	v_mul_f32_e32 v9, 0x437f0000, v9
	v_cvt_pk_u8_f32 v19, v1, 3, v0
	v_lshl_add_u64 v[0:1], v[24:25], 0, s[70:71]
	v_rndne_f32_e32 v11, v11
	v_rndne_f32_e32 v9, v9
	v_lshl_add_u64 v[0:1], v[0:1], 0, s[16:17]
	v_max_f32_e32 v11, 1.0, v11
	v_max_f32_e32 v9, 1.0, v9
	v_lshl_add_u64 v[0:1], v[0:1], 0, v[168:169]
	v_cvt_pk_u8_f32 v16, v11, 3, v10
	v_cvt_pk_u8_f32 v17, v9, 3, v8
	v_lshl_add_u64 v[20:21], v[0:1], 0, s[76:77]
	s_andn2_b64 vcc, exec, s[2:3]
	s_mov_b64 s[2:3], -1
	global_store_dwordx4 v[20:21], v[16:19], off
	s_cbranch_vccnz .LBB0_185
